# delete the per-phase s_setprio flips in both 8-phase GEMM K loops (A/B vs previous)
# speedup vs baseline: 1.0156x; 1.0101x over previous
.LBB2_21:
	ds_read_b128 v[150:153], v145
	ds_read_b128 v[154:157], v145 offset:1024
	ds_read_b128 v[158:161], v145 offset:2048
	ds_read_b128 v[162:165], v145 offset:3072
	s_add_i32 s65, s28, 2
	s_add_u32 s30, s26, 0x80
	s_addc_u32 s29, s27, 0
	s_cmp_eq_u32 s55, s28
	s_cselect_b32 s28, s4, s30
	s_cselect_b32 s29, s5, s29
	s_cselect_b32 s31, s7, s64
	s_cselect_b32 s30, s6, s63
	v_lshl_add_u64 v[142:143], s[26:27], 0, v[136:137]
	s_add_i32 m0, s43, 0xc000
	ds_read_b128 v[166:169], v146
	ds_read_b128 v[170:173], v146 offset:1024
	ds_read_b128 v[174:177], v146 offset:2048
	ds_read_b128 v[178:181], v146 offset:3072
	ds_read_b128 v[182:185], v146 offset:4096
	ds_read_b128 v[186:189], v146 offset:5120
	ds_read_b128 v[190:193], v146 offset:6144
	ds_read_b128 v[194:197], v146 offset:7168
	global_load_lds_dwordx4 v[142:143], off
	v_lshl_add_u64 v[142:143], s[26:27], 0, v[134:135]
	s_add_i32 m0, s43, 0xe000
	s_nop 0
	global_load_lds_dwordx4 v[142:143], off
	s_waitcnt lgkmcnt(8)
	s_barrier
	s_waitcnt lgkmcnt(0)
	s_waitcnt lgkmcnt(0)
	v_mfma_f32_16x16x32_f16 v[126:129], v[150:153], v[166:169], v[126:129]
	v_mfma_f32_16x16x32_f16 v[122:125], v[158:161], v[166:169], v[122:125]
	v_mfma_f32_16x16x32_f16 v[110:113], v[150:153], v[174:177], v[110:113]
	v_mfma_f32_16x16x32_f16 v[106:109], v[158:161], v[174:177], v[106:109]
	v_mfma_f32_16x16x32_f16 v[94:97], v[150:153], v[182:185], v[94:97]
	v_mfma_f32_16x16x32_f16 v[90:93], v[158:161], v[182:185], v[90:93]
	v_mfma_f32_16x16x32_f16 v[78:81], v[150:153], v[190:193], v[78:81]
	v_mfma_f32_16x16x32_f16 v[74:77], v[158:161], v[190:193], v[74:77]
	v_mfma_f32_16x16x32_f16 v[126:129], v[154:157], v[170:173], v[126:129]
	v_mfma_f32_16x16x32_f16 v[122:125], v[162:165], v[170:173], v[122:125]
	v_mfma_f32_16x16x32_f16 v[110:113], v[154:157], v[178:181], v[110:113]
	v_mfma_f32_16x16x32_f16 v[106:109], v[162:165], v[178:181], v[106:109]
	v_mfma_f32_16x16x32_f16 v[94:97], v[154:157], v[186:189], v[94:97]
	v_mfma_f32_16x16x32_f16 v[90:93], v[162:165], v[186:189], v[90:93]
	v_mfma_f32_16x16x32_f16 v[78:81], v[154:157], v[194:197], v[78:81]
	v_mfma_f32_16x16x32_f16 v[74:77], v[162:165], v[194:197], v[74:77]
	s_barrier
	s_add_i32 s66, s57, s40
	v_lshl_add_u64 v[142:143], s[30:31], 0, v[130:131]
	s_mov_b32 m0, s66
	ds_read_b128 v[198:201], v147
	ds_read_b128 v[202:205], v147 offset:1024
	ds_read_b128 v[206:209], v147 offset:2048
	ds_read_b128 v[210:213], v147 offset:3072
	global_load_lds_dwordx4 v[142:143], off
	v_lshl_add_u64 v[214:215], s[30:31], 0, v[132:133]
	s_add_i32 m0, s66, 0x2000
	s_nop 0
	global_load_lds_dwordx4 v[214:215], off
	s_barrier
	s_waitcnt lgkmcnt(0)
	s_waitcnt lgkmcnt(0)
	v_mfma_f32_16x16x32_f16 v[118:121], v[198:201], v[166:169], v[118:121]
	v_mfma_f32_16x16x32_f16 v[114:117], v[206:209], v[166:169], v[114:117]
	v_mfma_f32_16x16x32_f16 v[102:105], v[198:201], v[174:177], v[102:105]
	v_mfma_f32_16x16x32_f16 v[98:101], v[206:209], v[174:177], v[98:101]
	v_mfma_f32_16x16x32_f16 v[86:89], v[198:201], v[182:185], v[86:89]
	v_mfma_f32_16x16x32_f16 v[82:85], v[206:209], v[182:185], v[82:85]
	v_mfma_f32_16x16x32_f16 v[70:73], v[198:201], v[190:193], v[70:73]
	v_mfma_f32_16x16x32_f16 v[66:69], v[206:209], v[190:193], v[66:69]
	v_mfma_f32_16x16x32_f16 v[118:121], v[202:205], v[170:173], v[118:121]
	v_mfma_f32_16x16x32_f16 v[114:117], v[210:213], v[170:173], v[114:117]
	v_mfma_f32_16x16x32_f16 v[102:105], v[202:205], v[178:181], v[102:105]
	v_mfma_f32_16x16x32_f16 v[98:101], v[210:213], v[178:181], v[98:101]
	v_mfma_f32_16x16x32_f16 v[86:89], v[202:205], v[186:189], v[86:89]
	v_mfma_f32_16x16x32_f16 v[82:85], v[210:213], v[186:189], v[82:85]
	v_mfma_f32_16x16x32_f16 v[70:73], v[202:205], v[194:197], v[70:73]
	v_mfma_f32_16x16x32_f16 v[66:69], v[210:213], v[194:197], v[66:69]
	s_mov_b32 m0, s43
	v_lshl_add_u64 v[216:217], s[28:29], 0, v[130:131]
	s_barrier
	ds_read_b128 v[166:169], v146 offset:16384
	ds_read_b128 v[170:173], v146 offset:17408
	ds_read_b128 v[174:177], v146 offset:18432
	ds_read_b128 v[178:181], v146 offset:19456
	ds_read_b128 v[182:185], v146 offset:20480
	ds_read_b128 v[186:189], v146 offset:21504
	ds_read_b128 v[190:193], v146 offset:22528
	ds_read_b128 v[194:197], v146 offset:23552
	global_load_lds_dwordx4 v[216:217], off
	v_lshl_add_u64 v[218:219], s[28:29], 0, v[132:133]
	s_mov_b32 m0, s44
	s_nop 0
	global_load_lds_dwordx4 v[218:219], off
	s_barrier
	s_waitcnt lgkmcnt(0)
	s_waitcnt lgkmcnt(0)
	v_mfma_f32_16x16x32_f16 v[62:65], v[150:153], v[166:169], v[62:65]
	v_mfma_f32_16x16x32_f16 v[58:61], v[158:161], v[166:169], v[58:61]
	v_mfma_f32_16x16x32_f16 v[46:49], v[150:153], v[174:177], v[46:49]
	v_mfma_f32_16x16x32_f16 v[42:45], v[158:161], v[174:177], v[42:45]
	v_mfma_f32_16x16x32_f16 v[30:33], v[150:153], v[182:185], v[30:33]
	v_mfma_f32_16x16x32_f16 v[26:29], v[158:161], v[182:185], v[26:29]
	v_mfma_f32_16x16x32_f16 v[14:17], v[150:153], v[190:193], v[14:17]
	v_mfma_f32_16x16x32_f16 v[10:13], v[158:161], v[190:193], v[10:13]
	v_mfma_f32_16x16x32_f16 v[62:65], v[154:157], v[170:173], v[62:65]
	v_mfma_f32_16x16x32_f16 v[58:61], v[162:165], v[170:173], v[58:61]
	v_mfma_f32_16x16x32_f16 v[46:49], v[154:157], v[178:181], v[46:49]
	v_mfma_f32_16x16x32_f16 v[42:45], v[162:165], v[178:181], v[42:45]
	v_mfma_f32_16x16x32_f16 v[30:33], v[154:157], v[186:189], v[30:33]
	v_mfma_f32_16x16x32_f16 v[26:29], v[162:165], v[186:189], v[26:29]
	v_mfma_f32_16x16x32_f16 v[14:17], v[154:157], v[194:197], v[14:17]
	v_mfma_f32_16x16x32_f16 v[10:13], v[162:165], v[194:197], v[10:13]
	s_barrier
	s_add_u32 s30, s30, s10
	s_addc_u32 s31, s31, s11
	s_add_i32 s66, s58, s40
	v_lshl_add_u64 v[220:221], s[30:31], 0, v[130:131]
	s_mov_b32 m0, s66
	v_lshl_add_u64 v[222:223], s[30:31], 0, v[132:133]
	global_load_lds_dwordx4 v[220:221], off
	s_add_i32 m0, s66, 0x2000
	s_nop 0
	global_load_lds_dwordx4 v[222:223], off
	s_waitcnt vmcnt(6)
	s_barrier
	v_mfma_f32_16x16x32_f16 v[54:57], v[198:201], v[166:169], v[54:57]
	v_mfma_f32_16x16x32_f16 v[50:53], v[206:209], v[166:169], v[50:53]
	v_mfma_f32_16x16x32_f16 v[38:41], v[198:201], v[174:177], v[38:41]
	v_mfma_f32_16x16x32_f16 v[34:37], v[206:209], v[174:177], v[34:37]
	v_mfma_f32_16x16x32_f16 v[22:25], v[198:201], v[182:185], v[22:25]
	v_mfma_f32_16x16x32_f16 v[18:21], v[206:209], v[182:185], v[18:21]
	v_mfma_f32_16x16x32_f16 v[6:9], v[198:201], v[190:193], v[6:9]
	v_mfma_f32_16x16x32_f16 v[2:5], v[206:209], v[190:193], v[2:5]
	v_mfma_f32_16x16x32_f16 v[54:57], v[202:205], v[170:173], v[54:57]
	v_mfma_f32_16x16x32_f16 v[50:53], v[210:213], v[170:173], v[50:53]
	v_mfma_f32_16x16x32_f16 v[38:41], v[202:205], v[178:181], v[38:41]
	v_mfma_f32_16x16x32_f16 v[34:37], v[210:213], v[178:181], v[34:37]
	v_mfma_f32_16x16x32_f16 v[22:25], v[202:205], v[186:189], v[22:25]
	v_mfma_f32_16x16x32_f16 v[18:21], v[210:213], v[186:189], v[18:21]
	v_mfma_f32_16x16x32_f16 v[6:9], v[202:205], v[194:197], v[6:9]
	v_mfma_f32_16x16x32_f16 v[2:5], v[210:213], v[194:197], v[2:5]
	s_add_i32 s30, 0, 0x18000
	v_add_u32_e32 v140, s30, v141
	s_barrier
	ds_read_b128 v[150:153], v140
	ds_read_b128 v[154:157], v140 offset:1024
	ds_read_b128 v[158:161], v140 offset:2048
	ds_read_b128 v[162:165], v140 offset:3072
	s_add_u32 s28, s28, s10
	s_addc_u32 s29, s29, s11
	s_mov_b32 m0, s45
	v_lshl_add_u64 v[198:199], s[28:29], 0, v[130:131]
	ds_read_b128 v[166:169], v146 offset:32768
	ds_read_b128 v[170:173], v146 offset:33792
	ds_read_b128 v[174:177], v146 offset:34816
	ds_read_b128 v[178:181], v146 offset:35840
	ds_read_b128 v[182:185], v146 offset:36864
	ds_read_b128 v[186:189], v146 offset:37888
	ds_read_b128 v[190:193], v146 offset:38912
	ds_read_b128 v[194:197], v146 offset:39936
	global_load_lds_dwordx4 v[198:199], off
	v_lshl_add_u64 v[198:199], s[28:29], 0, v[132:133]
	s_mov_b32 m0, s46
	s_nop 0
	global_load_lds_dwordx4 v[198:199], off
	s_waitcnt lgkmcnt(8)
	s_barrier
	s_waitcnt lgkmcnt(0)
	s_waitcnt lgkmcnt(0)
	v_mfma_f32_16x16x32_f16 v[126:129], v[150:153], v[166:169], v[126:129]
	v_mfma_f32_16x16x32_f16 v[122:125], v[158:161], v[166:169], v[122:125]
	v_mfma_f32_16x16x32_f16 v[110:113], v[150:153], v[174:177], v[110:113]
	v_mfma_f32_16x16x32_f16 v[106:109], v[158:161], v[174:177], v[106:109]
	v_mfma_f32_16x16x32_f16 v[94:97], v[150:153], v[182:185], v[94:97]
	v_mfma_f32_16x16x32_f16 v[90:93], v[158:161], v[182:185], v[90:93]
	v_mfma_f32_16x16x32_f16 v[78:81], v[150:153], v[190:193], v[78:81]
	v_mfma_f32_16x16x32_f16 v[74:77], v[158:161], v[190:193], v[74:77]
	v_mfma_f32_16x16x32_f16 v[126:129], v[154:157], v[170:173], v[126:129]
	v_mfma_f32_16x16x32_f16 v[122:125], v[162:165], v[170:173], v[122:125]
	v_mfma_f32_16x16x32_f16 v[110:113], v[154:157], v[178:181], v[110:113]
	v_mfma_f32_16x16x32_f16 v[106:109], v[162:165], v[178:181], v[106:109]
	v_mfma_f32_16x16x32_f16 v[94:97], v[154:157], v[186:189], v[94:97]
	v_mfma_f32_16x16x32_f16 v[90:93], v[162:165], v[186:189], v[90:93]
	v_mfma_f32_16x16x32_f16 v[78:81], v[154:157], v[194:197], v[78:81]
	v_mfma_f32_16x16x32_f16 v[74:77], v[162:165], v[194:197], v[74:77]
	s_barrier
	s_add_i32 s28, 0, 0x1c000
	s_add_i32 s29, s30, s40
	v_add_u32_e32 v140, s28, v141
	v_lshl_add_u64 v[142:143], v[142:143], 0, s[22:23]
	s_mov_b32 m0, s29
	ds_read_b128 v[198:201], v140
	ds_read_b128 v[202:205], v140 offset:1024
	ds_read_b128 v[206:209], v140 offset:2048
	ds_read_b128 v[210:213], v140 offset:3072
	global_load_lds_dwordx4 v[142:143], off
	v_lshl_add_u64 v[142:143], v[214:215], 0, s[22:23]
	s_add_i32 m0, s29, 0x2000
	s_nop 0
	global_load_lds_dwordx4 v[142:143], off
	s_barrier
	s_waitcnt lgkmcnt(0)
	s_waitcnt lgkmcnt(0)
	v_mfma_f32_16x16x32_f16 v[118:121], v[198:201], v[166:169], v[118:121]
	v_mfma_f32_16x16x32_f16 v[114:117], v[206:209], v[166:169], v[114:117]
	v_mfma_f32_16x16x32_f16 v[102:105], v[198:201], v[174:177], v[102:105]
	v_mfma_f32_16x16x32_f16 v[98:101], v[206:209], v[174:177], v[98:101]
	v_mfma_f32_16x16x32_f16 v[86:89], v[198:201], v[182:185], v[86:89]
	v_mfma_f32_16x16x32_f16 v[82:85], v[206:209], v[182:185], v[82:85]
	v_mfma_f32_16x16x32_f16 v[70:73], v[198:201], v[190:193], v[70:73]
	v_mfma_f32_16x16x32_f16 v[66:69], v[206:209], v[190:193], v[66:69]
	v_mfma_f32_16x16x32_f16 v[118:121], v[202:205], v[170:173], v[118:121]
	v_mfma_f32_16x16x32_f16 v[114:117], v[210:213], v[170:173], v[114:117]
	v_mfma_f32_16x16x32_f16 v[102:105], v[202:205], v[178:181], v[102:105]
	v_mfma_f32_16x16x32_f16 v[98:101], v[210:213], v[178:181], v[98:101]
	v_mfma_f32_16x16x32_f16 v[86:89], v[202:205], v[186:189], v[86:89]
	v_mfma_f32_16x16x32_f16 v[82:85], v[210:213], v[186:189], v[82:85]
	v_mfma_f32_16x16x32_f16 v[70:73], v[202:205], v[194:197], v[70:73]
	v_mfma_f32_16x16x32_f16 v[66:69], v[210:213], v[194:197], v[66:69]
	s_mov_b32 m0, s49
	v_lshl_add_u64 v[142:143], v[216:217], 0, s[22:23]
	s_barrier
	ds_read_b128 v[166:169], v146 offset:49152
	ds_read_b128 v[170:173], v146 offset:50176
	ds_read_b128 v[174:177], v146 offset:51200
	ds_read_b128 v[178:181], v146 offset:52224
	ds_read_b128 v[182:185], v146 offset:53248
	ds_read_b128 v[186:189], v146 offset:54272
	ds_read_b128 v[190:193], v146 offset:55296
	ds_read_b128 v[194:197], v146 offset:56320
	global_load_lds_dwordx4 v[142:143], off
	v_lshl_add_u64 v[142:143], v[218:219], 0, s[22:23]
	s_mov_b32 m0, s50
	s_nop 0
	global_load_lds_dwordx4 v[142:143], off
	s_barrier
	s_waitcnt lgkmcnt(0)
	s_waitcnt lgkmcnt(0)
	v_mfma_f32_16x16x32_f16 v[62:65], v[150:153], v[166:169], v[62:65]
	v_mfma_f32_16x16x32_f16 v[58:61], v[158:161], v[166:169], v[58:61]
	v_mfma_f32_16x16x32_f16 v[46:49], v[150:153], v[174:177], v[46:49]
	v_mfma_f32_16x16x32_f16 v[42:45], v[158:161], v[174:177], v[42:45]
	v_mfma_f32_16x16x32_f16 v[30:33], v[150:153], v[182:185], v[30:33]
	v_mfma_f32_16x16x32_f16 v[26:29], v[158:161], v[182:185], v[26:29]
	v_mfma_f32_16x16x32_f16 v[14:17], v[150:153], v[190:193], v[14:17]
	v_mfma_f32_16x16x32_f16 v[10:13], v[158:161], v[190:193], v[10:13]
	v_mfma_f32_16x16x32_f16 v[62:65], v[154:157], v[170:173], v[62:65]
	v_mfma_f32_16x16x32_f16 v[58:61], v[162:165], v[170:173], v[58:61]
	v_mfma_f32_16x16x32_f16 v[46:49], v[154:157], v[178:181], v[46:49]
	v_mfma_f32_16x16x32_f16 v[42:45], v[162:165], v[178:181], v[42:45]
	v_mfma_f32_16x16x32_f16 v[30:33], v[154:157], v[186:189], v[30:33]
	v_mfma_f32_16x16x32_f16 v[26:29], v[162:165], v[186:189], v[26:29]
	v_mfma_f32_16x16x32_f16 v[14:17], v[154:157], v[194:197], v[14:17]
	v_mfma_f32_16x16x32_f16 v[10:13], v[162:165], v[194:197], v[10:13]
	s_barrier
	s_add_i32 s28, s28, s40
	v_lshl_add_u64 v[142:143], v[220:221], 0, s[22:23]
	s_mov_b32 m0, s28
	s_nop 0
	global_load_lds_dwordx4 v[142:143], off
	v_lshl_add_u64 v[142:143], v[222:223], 0, s[22:23]
	s_add_i32 m0, s28, 0x2000
	s_nop 0
	global_load_lds_dwordx4 v[142:143], off
	s_waitcnt vmcnt(6)
	s_barrier
	v_mfma_f32_16x16x32_f16 v[54:57], v[198:201], v[166:169], v[54:57]
	v_mfma_f32_16x16x32_f16 v[50:53], v[206:209], v[166:169], v[50:53]
	v_mfma_f32_16x16x32_f16 v[38:41], v[198:201], v[174:177], v[38:41]
	v_mfma_f32_16x16x32_f16 v[34:37], v[206:209], v[174:177], v[34:37]
	v_mfma_f32_16x16x32_f16 v[22:25], v[198:201], v[182:185], v[22:25]
	v_mfma_f32_16x16x32_f16 v[18:21], v[206:209], v[182:185], v[18:21]
	v_mfma_f32_16x16x32_f16 v[6:9], v[198:201], v[190:193], v[6:9]
	v_mfma_f32_16x16x32_f16 v[2:5], v[206:209], v[190:193], v[2:5]
	v_mfma_f32_16x16x32_f16 v[54:57], v[202:205], v[170:173], v[54:57]
	v_mfma_f32_16x16x32_f16 v[50:53], v[210:213], v[170:173], v[50:53]
	v_mfma_f32_16x16x32_f16 v[38:41], v[202:205], v[178:181], v[38:41]
	v_mfma_f32_16x16x32_f16 v[34:37], v[210:213], v[178:181], v[34:37]
	v_mfma_f32_16x16x32_f16 v[22:25], v[202:205], v[186:189], v[22:25]
	v_mfma_f32_16x16x32_f16 v[18:21], v[210:213], v[186:189], v[18:21]
	v_mfma_f32_16x16x32_f16 v[6:9], v[202:205], v[194:197], v[6:9]
	v_mfma_f32_16x16x32_f16 v[2:5], v[210:213], v[194:197], v[2:5]
	s_add_u32 s63, s63, 0x100
	s_addc_u32 s64, s64, 0
	s_add_u32 s26, s26, 0x100
	s_addc_u32 s27, s27, 0
	s_cmp_ge_i32 s65, s51
	s_mov_b32 s28, s65
	s_barrier
	s_cbranch_scc0 .LBB2_21
	s_branch .LBB2_8

.LBB3_23:
	ds_read_b128 v[128:131], v169
	ds_read_b128 v[132:135], v169 offset:1024
	ds_read_b128 v[136:139], v169 offset:2048
	ds_read_b128 v[140:143], v169 offset:3072
	s_add_i32 s71, s34, 2
	s_add_u32 s36, s30, 0x80
	s_addc_u32 s35, s31, 0
	s_cmp_eq_u32 s62, s34
	s_cselect_b32 s34, s28, s36
	s_cselect_b32 s35, s29, s35
	s_cselect_b32 s37, s5, s70
	s_cselect_b32 s36, s4, s69
	v_lshl_add_u64 v[200:201], s[30:31], 0, v[150:151]
	s_add_i32 m0, s51, 0xc000
	ds_read_b128 v[154:157], v170
	ds_read_b128 v[172:175], v170 offset:1024
	ds_read_b128 v[176:179], v170 offset:2048
	ds_read_b128 v[180:183], v170 offset:3072
	ds_read_b128 v[184:187], v170 offset:4096
	ds_read_b128 v[188:191], v170 offset:5120
	ds_read_b128 v[192:195], v170 offset:6144
	ds_read_b128 v[196:199], v170 offset:7168
	global_load_lds_dwordx4 v[200:201], off
	v_lshl_add_u64 v[200:201], s[30:31], 0, v[148:149]
	s_add_i32 m0, s51, 0xe000
	s_nop 0
	global_load_lds_dwordx4 v[200:201], off
	s_waitcnt lgkmcnt(8)
	s_barrier
	s_waitcnt lgkmcnt(0)
	s_waitcnt lgkmcnt(0)
	v_mfma_f32_16x16x32_f16 v[116:119], v[128:131], v[154:157], v[116:119]
	v_mfma_f32_16x16x32_f16 v[124:127], v[136:139], v[154:157], v[124:127]
	v_mfma_f32_16x16x32_f16 v[108:111], v[128:131], v[176:179], v[108:111]
	v_mfma_f32_16x16x32_f16 v[104:107], v[136:139], v[176:179], v[104:107]
	v_mfma_f32_16x16x32_f16 v[92:95], v[128:131], v[184:187], v[92:95]
	v_mfma_f32_16x16x32_f16 v[88:91], v[136:139], v[184:187], v[88:91]
	v_mfma_f32_16x16x32_f16 v[76:79], v[128:131], v[192:195], v[76:79]
	v_mfma_f32_16x16x32_f16 v[72:75], v[136:139], v[192:195], v[72:75]
	v_mfma_f32_16x16x32_f16 v[116:119], v[132:135], v[172:175], v[116:119]
	v_mfma_f32_16x16x32_f16 v[124:127], v[140:143], v[172:175], v[124:127]
	v_mfma_f32_16x16x32_f16 v[108:111], v[132:135], v[180:183], v[108:111]
	v_mfma_f32_16x16x32_f16 v[104:107], v[140:143], v[180:183], v[104:107]
	v_mfma_f32_16x16x32_f16 v[92:95], v[132:135], v[188:191], v[92:95]
	v_mfma_f32_16x16x32_f16 v[88:91], v[140:143], v[188:191], v[88:91]
	v_mfma_f32_16x16x32_f16 v[76:79], v[132:135], v[196:199], v[76:79]
	v_mfma_f32_16x16x32_f16 v[72:75], v[140:143], v[196:199], v[72:75]
	s_barrier
	s_add_i32 s72, s63, s40
	v_lshl_add_u64 v[216:217], s[36:37], 0, v[144:145]
	s_mov_b32 m0, s72
	ds_read_b128 v[200:203], v171
	ds_read_b128 v[204:207], v171 offset:1024
	ds_read_b128 v[208:211], v171 offset:2048
	ds_read_b128 v[212:215], v171 offset:3072
	global_load_lds_dwordx4 v[216:217], off
	v_lshl_add_u64 v[218:219], s[36:37], 0, v[146:147]
	s_add_i32 m0, s72, 0x2000
	s_nop 0
	global_load_lds_dwordx4 v[218:219], off
	s_barrier
	s_waitcnt lgkmcnt(0)
	s_waitcnt lgkmcnt(0)
	v_mfma_f32_16x16x32_f16 v[120:123], v[200:203], v[154:157], v[120:123]
	v_mfma_f32_16x16x32_f16 v[112:115], v[208:211], v[154:157], v[112:115]
	v_mfma_f32_16x16x32_f16 v[100:103], v[200:203], v[176:179], v[100:103]
	v_mfma_f32_16x16x32_f16 v[96:99], v[208:211], v[176:179], v[96:99]
	v_mfma_f32_16x16x32_f16 v[84:87], v[200:203], v[184:187], v[84:87]
	v_mfma_f32_16x16x32_f16 v[80:83], v[208:211], v[184:187], v[80:83]
	v_mfma_f32_16x16x32_f16 v[68:71], v[200:203], v[192:195], v[68:71]
	v_mfma_f32_16x16x32_f16 v[64:67], v[208:211], v[192:195], v[64:67]
	v_mfma_f32_16x16x32_f16 v[120:123], v[204:207], v[172:175], v[120:123]
	v_mfma_f32_16x16x32_f16 v[112:115], v[212:215], v[172:175], v[112:115]
	v_mfma_f32_16x16x32_f16 v[100:103], v[204:207], v[180:183], v[100:103]
	v_mfma_f32_16x16x32_f16 v[96:99], v[212:215], v[180:183], v[96:99]
	v_mfma_f32_16x16x32_f16 v[84:87], v[204:207], v[188:191], v[84:87]
	v_mfma_f32_16x16x32_f16 v[80:83], v[212:215], v[188:191], v[80:83]
	v_mfma_f32_16x16x32_f16 v[68:71], v[204:207], v[196:199], v[68:71]
	v_mfma_f32_16x16x32_f16 v[64:67], v[212:215], v[196:199], v[64:67]
	s_mov_b32 m0, s51
	v_lshl_add_u64 v[220:221], s[34:35], 0, v[144:145]
	s_barrier
	ds_read_b128 v[154:157], v170 offset:16384
	ds_read_b128 v[172:175], v170 offset:17408
	ds_read_b128 v[176:179], v170 offset:18432
	ds_read_b128 v[180:183], v170 offset:19456
	ds_read_b128 v[184:187], v170 offset:20480
	ds_read_b128 v[188:191], v170 offset:21504
	ds_read_b128 v[192:195], v170 offset:22528
	ds_read_b128 v[196:199], v170 offset:23552
	global_load_lds_dwordx4 v[220:221], off
	v_lshl_add_u64 v[222:223], s[34:35], 0, v[146:147]
	s_mov_b32 m0, s52
	s_nop 0
	global_load_lds_dwordx4 v[222:223], off
	s_barrier
	s_waitcnt lgkmcnt(0)
	s_waitcnt lgkmcnt(0)
	v_mfma_f32_16x16x32_f16 v[60:63], v[128:131], v[154:157], v[60:63]
	v_mfma_f32_16x16x32_f16 v[56:59], v[136:139], v[154:157], v[56:59]
	v_mfma_f32_16x16x32_f16 v[44:47], v[128:131], v[176:179], v[44:47]
	v_mfma_f32_16x16x32_f16 v[40:43], v[136:139], v[176:179], v[40:43]
	v_mfma_f32_16x16x32_f16 v[28:31], v[128:131], v[184:187], v[28:31]
	v_mfma_f32_16x16x32_f16 v[24:27], v[136:139], v[184:187], v[24:27]
	v_mfma_f32_16x16x32_f16 v[12:15], v[128:131], v[192:195], v[12:15]
	v_mfma_f32_16x16x32_f16 v[8:11], v[136:139], v[192:195], v[8:11]
	v_mfma_f32_16x16x32_f16 v[60:63], v[132:135], v[172:175], v[60:63]
	v_mfma_f32_16x16x32_f16 v[56:59], v[140:143], v[172:175], v[56:59]
	v_mfma_f32_16x16x32_f16 v[44:47], v[132:135], v[180:183], v[44:47]
	v_mfma_f32_16x16x32_f16 v[40:43], v[140:143], v[180:183], v[40:43]
	v_mfma_f32_16x16x32_f16 v[28:31], v[132:135], v[188:191], v[28:31]
	v_mfma_f32_16x16x32_f16 v[24:27], v[140:143], v[188:191], v[24:27]
	v_mfma_f32_16x16x32_f16 v[12:15], v[132:135], v[196:199], v[12:15]
	v_mfma_f32_16x16x32_f16 v[8:11], v[140:143], v[196:199], v[8:11]
	s_barrier
	s_add_u32 s36, s36, s20
	s_addc_u32 s37, s37, s21
	s_add_i32 s72, s64, s40
	v_lshl_add_u64 v[224:225], s[36:37], 0, v[144:145]
	s_mov_b32 m0, s72
	v_lshl_add_u64 v[226:227], s[36:37], 0, v[146:147]
	global_load_lds_dwordx4 v[224:225], off
	s_add_i32 m0, s72, 0x2000
	s_nop 0
	global_load_lds_dwordx4 v[226:227], off
	s_waitcnt vmcnt(6)
	s_barrier
	v_mfma_f32_16x16x32_f16 v[52:55], v[200:203], v[154:157], v[52:55]
	v_mfma_f32_16x16x32_f16 v[48:51], v[208:211], v[154:157], v[48:51]
	v_mfma_f32_16x16x32_f16 v[36:39], v[200:203], v[176:179], v[36:39]
	v_mfma_f32_16x16x32_f16 v[32:35], v[208:211], v[176:179], v[32:35]
	v_mfma_f32_16x16x32_f16 v[20:23], v[200:203], v[184:187], v[20:23]
	v_mfma_f32_16x16x32_f16 v[16:19], v[208:211], v[184:187], v[16:19]
	v_mfma_f32_16x16x32_f16 v[4:7], v[200:203], v[192:195], v[4:7]
	v_mfma_f32_16x16x32_f16 v[0:3], v[208:211], v[192:195], v[0:3]
	v_mfma_f32_16x16x32_f16 v[52:55], v[204:207], v[172:175], v[52:55]
	v_mfma_f32_16x16x32_f16 v[48:51], v[212:215], v[172:175], v[48:51]
	v_mfma_f32_16x16x32_f16 v[36:39], v[204:207], v[180:183], v[36:39]
	v_mfma_f32_16x16x32_f16 v[32:35], v[212:215], v[180:183], v[32:35]
	v_mfma_f32_16x16x32_f16 v[20:23], v[204:207], v[188:191], v[20:23]
	v_mfma_f32_16x16x32_f16 v[16:19], v[212:215], v[188:191], v[16:19]
	v_mfma_f32_16x16x32_f16 v[4:7], v[204:207], v[196:199], v[4:7]
	v_mfma_f32_16x16x32_f16 v[0:3], v[212:215], v[196:199], v[0:3]
	s_add_i32 s36, 0, 0x18000
	v_add_u32_e32 v140, s36, v161
	s_barrier
	ds_read_b128 v[128:131], v140
	ds_read_b128 v[132:135], v140 offset:1024
	ds_read_b128 v[136:139], v140 offset:2048
	ds_read_b128 v[140:143], v140 offset:3072
	s_add_u32 s34, s34, s20
	s_addc_u32 s35, s35, s21
	s_mov_b32 m0, s53
	v_lshl_add_u64 v[200:201], s[34:35], 0, v[144:145]
	ds_read_b128 v[154:157], v170 offset:32768
	ds_read_b128 v[172:175], v170 offset:33792
	ds_read_b128 v[176:179], v170 offset:34816
	ds_read_b128 v[180:183], v170 offset:35840
	ds_read_b128 v[184:187], v170 offset:36864
	ds_read_b128 v[188:191], v170 offset:37888
	ds_read_b128 v[192:195], v170 offset:38912
	ds_read_b128 v[196:199], v170 offset:39936
	global_load_lds_dwordx4 v[200:201], off
	v_lshl_add_u64 v[200:201], s[34:35], 0, v[146:147]
	s_mov_b32 m0, s54
	s_nop 0
	global_load_lds_dwordx4 v[200:201], off
	s_waitcnt lgkmcnt(8)
	s_barrier
	s_waitcnt lgkmcnt(0)
	s_waitcnt lgkmcnt(0)
	v_mfma_f32_16x16x32_f16 v[116:119], v[128:131], v[154:157], v[116:119]
	v_mfma_f32_16x16x32_f16 v[124:127], v[136:139], v[154:157], v[124:127]
	v_mfma_f32_16x16x32_f16 v[108:111], v[128:131], v[176:179], v[108:111]
	v_mfma_f32_16x16x32_f16 v[104:107], v[136:139], v[176:179], v[104:107]
	v_mfma_f32_16x16x32_f16 v[92:95], v[128:131], v[184:187], v[92:95]
	v_mfma_f32_16x16x32_f16 v[88:91], v[136:139], v[184:187], v[88:91]
	v_mfma_f32_16x16x32_f16 v[76:79], v[128:131], v[192:195], v[76:79]
	v_mfma_f32_16x16x32_f16 v[72:75], v[136:139], v[192:195], v[72:75]
	v_mfma_f32_16x16x32_f16 v[116:119], v[132:135], v[172:175], v[116:119]
	v_mfma_f32_16x16x32_f16 v[124:127], v[140:143], v[172:175], v[124:127]
	v_mfma_f32_16x16x32_f16 v[108:111], v[132:135], v[180:183], v[108:111]
	v_mfma_f32_16x16x32_f16 v[104:107], v[140:143], v[180:183], v[104:107]
	v_mfma_f32_16x16x32_f16 v[92:95], v[132:135], v[188:191], v[92:95]
	v_mfma_f32_16x16x32_f16 v[88:91], v[140:143], v[188:191], v[88:91]
	v_mfma_f32_16x16x32_f16 v[76:79], v[132:135], v[196:199], v[76:79]
	v_mfma_f32_16x16x32_f16 v[72:75], v[140:143], v[196:199], v[72:75]
	s_barrier
	s_add_i32 s34, 0, 0x1c000
	s_add_i32 s35, s36, s40
	v_add_u32_e32 v212, s34, v161
	v_lshl_add_u64 v[216:217], v[216:217], 0, s[24:25]
	s_mov_b32 m0, s35
	ds_read_b128 v[200:203], v212
	ds_read_b128 v[204:207], v212 offset:1024
	ds_read_b128 v[208:211], v212 offset:2048
	ds_read_b128 v[212:215], v212 offset:3072
	global_load_lds_dwordx4 v[216:217], off
	v_lshl_add_u64 v[216:217], v[218:219], 0, s[24:25]
	s_add_i32 m0, s35, 0x2000
	s_nop 0
	global_load_lds_dwordx4 v[216:217], off
	s_barrier
	s_waitcnt lgkmcnt(0)
	s_waitcnt lgkmcnt(0)
	v_mfma_f32_16x16x32_f16 v[120:123], v[200:203], v[154:157], v[120:123]
	v_mfma_f32_16x16x32_f16 v[112:115], v[208:211], v[154:157], v[112:115]
	v_mfma_f32_16x16x32_f16 v[100:103], v[200:203], v[176:179], v[100:103]
	v_mfma_f32_16x16x32_f16 v[96:99], v[208:211], v[176:179], v[96:99]
	v_mfma_f32_16x16x32_f16 v[84:87], v[200:203], v[184:187], v[84:87]
	v_mfma_f32_16x16x32_f16 v[80:83], v[208:211], v[184:187], v[80:83]
	v_mfma_f32_16x16x32_f16 v[68:71], v[200:203], v[192:195], v[68:71]
	v_mfma_f32_16x16x32_f16 v[64:67], v[208:211], v[192:195], v[64:67]
	v_mfma_f32_16x16x32_f16 v[120:123], v[204:207], v[172:175], v[120:123]
	v_mfma_f32_16x16x32_f16 v[112:115], v[212:215], v[172:175], v[112:115]
	v_mfma_f32_16x16x32_f16 v[100:103], v[204:207], v[180:183], v[100:103]
	v_mfma_f32_16x16x32_f16 v[96:99], v[212:215], v[180:183], v[96:99]
	v_mfma_f32_16x16x32_f16 v[84:87], v[204:207], v[188:191], v[84:87]
	v_mfma_f32_16x16x32_f16 v[80:83], v[212:215], v[188:191], v[80:83]
	v_mfma_f32_16x16x32_f16 v[68:71], v[204:207], v[196:199], v[68:71]
	v_mfma_f32_16x16x32_f16 v[64:67], v[212:215], v[196:199], v[64:67]
	s_mov_b32 m0, s57
	v_lshl_add_u64 v[216:217], v[220:221], 0, s[24:25]
	s_barrier
	ds_read_b128 v[154:157], v170 offset:49152
	ds_read_b128 v[172:175], v170 offset:50176
	ds_read_b128 v[176:179], v170 offset:51200
	ds_read_b128 v[180:183], v170 offset:52224
	ds_read_b128 v[184:187], v170 offset:53248
	ds_read_b128 v[188:191], v170 offset:54272
	ds_read_b128 v[192:195], v170 offset:55296
	ds_read_b128 v[196:199], v170 offset:56320
	global_load_lds_dwordx4 v[216:217], off
	v_lshl_add_u64 v[216:217], v[222:223], 0, s[24:25]
	s_mov_b32 m0, s58
	s_nop 0
	global_load_lds_dwordx4 v[216:217], off
	s_barrier
	s_waitcnt lgkmcnt(0)
	s_waitcnt lgkmcnt(0)
	v_mfma_f32_16x16x32_f16 v[60:63], v[128:131], v[154:157], v[60:63]
	v_mfma_f32_16x16x32_f16 v[56:59], v[136:139], v[154:157], v[56:59]
	v_mfma_f32_16x16x32_f16 v[44:47], v[128:131], v[176:179], v[44:47]
	v_mfma_f32_16x16x32_f16 v[40:43], v[136:139], v[176:179], v[40:43]
	v_mfma_f32_16x16x32_f16 v[28:31], v[128:131], v[184:187], v[28:31]
	v_mfma_f32_16x16x32_f16 v[24:27], v[136:139], v[184:187], v[24:27]
	v_mfma_f32_16x16x32_f16 v[12:15], v[128:131], v[192:195], v[12:15]
	v_mfma_f32_16x16x32_f16 v[8:11], v[136:139], v[192:195], v[8:11]
	v_mfma_f32_16x16x32_f16 v[60:63], v[132:135], v[172:175], v[60:63]
	v_mfma_f32_16x16x32_f16 v[56:59], v[140:143], v[172:175], v[56:59]
	v_mfma_f32_16x16x32_f16 v[44:47], v[132:135], v[180:183], v[44:47]
	v_mfma_f32_16x16x32_f16 v[40:43], v[140:143], v[180:183], v[40:43]
	v_mfma_f32_16x16x32_f16 v[28:31], v[132:135], v[188:191], v[28:31]
	v_mfma_f32_16x16x32_f16 v[24:27], v[140:143], v[188:191], v[24:27]
	v_mfma_f32_16x16x32_f16 v[12:15], v[132:135], v[196:199], v[12:15]
	v_mfma_f32_16x16x32_f16 v[8:11], v[140:143], v[196:199], v[8:11]
	s_barrier
	s_add_i32 s34, s34, s40
	v_lshl_add_u64 v[128:129], v[224:225], 0, s[24:25]
	s_mov_b32 m0, s34
	s_nop 0
	global_load_lds_dwordx4 v[128:129], off
	v_lshl_add_u64 v[128:129], v[226:227], 0, s[24:25]
	s_add_i32 m0, s34, 0x2000
	s_nop 0
	global_load_lds_dwordx4 v[128:129], off
	s_waitcnt vmcnt(6)
	s_barrier
	v_mfma_f32_16x16x32_f16 v[52:55], v[200:203], v[154:157], v[52:55]
	v_mfma_f32_16x16x32_f16 v[48:51], v[208:211], v[154:157], v[48:51]
	v_mfma_f32_16x16x32_f16 v[36:39], v[200:203], v[176:179], v[36:39]
	v_mfma_f32_16x16x32_f16 v[32:35], v[208:211], v[176:179], v[32:35]
	v_mfma_f32_16x16x32_f16 v[20:23], v[200:203], v[184:187], v[20:23]
	v_mfma_f32_16x16x32_f16 v[16:19], v[208:211], v[184:187], v[16:19]
	v_mfma_f32_16x16x32_f16 v[4:7], v[200:203], v[192:195], v[4:7]
	v_mfma_f32_16x16x32_f16 v[0:3], v[208:211], v[192:195], v[0:3]
	v_mfma_f32_16x16x32_f16 v[52:55], v[204:207], v[172:175], v[52:55]
	v_mfma_f32_16x16x32_f16 v[48:51], v[212:215], v[172:175], v[48:51]
	v_mfma_f32_16x16x32_f16 v[36:39], v[204:207], v[180:183], v[36:39]
	v_mfma_f32_16x16x32_f16 v[32:35], v[212:215], v[180:183], v[32:35]
	v_mfma_f32_16x16x32_f16 v[20:23], v[204:207], v[188:191], v[20:23]
	v_mfma_f32_16x16x32_f16 v[16:19], v[212:215], v[188:191], v[16:19]
	v_mfma_f32_16x16x32_f16 v[4:7], v[204:207], v[196:199], v[4:7]
	v_mfma_f32_16x16x32_f16 v[0:3], v[212:215], v[196:199], v[0:3]
	s_add_u32 s69, s69, 0x100
	s_addc_u32 s70, s70, 0
	s_add_u32 s30, s30, 0x100
	s_addc_u32 s31, s31, 0
	s_cmp_ge_i32 s71, s39
	s_mov_b32 s34, s71
	s_barrier
	s_cbranch_scc0 .LBB3_23
	s_branch .LBB3_10
